# B3 preamble: router-weight x gain LDS fill loop rewritten to issue its 16 loads per iteration together (was 4 serialized load groups)
# speedup vs baseline: 1.0037x; 1.0037x over previous
.LBB0_1297:
	s_waitcnt vmcnt(14)
	v_mov_b32_e32 v9, 0
	v_mov_b32_e32 v11, 0
	v_mov_b32_e32 v8, v2
	v_mov_b32_e32 v10, v3
	v_lshl_add_u64 v[16:17], v[8:9], 2, s[18:19]
	global_load_dword v236, v[16:17], off
	v_lshl_add_u64 v[16:17], v[10:11], 2, s[18:19]
	global_load_dword v240, v[16:17], off
	v_ashrrev_i32_e32 v8, 3, v8
	v_ashrrev_i32_e32 v10, 3, v10
	v_lshl_add_u64 v[16:17], v[8:9], 2, s[0:1]
	global_load_dword v244, v[16:17], off
	v_lshl_add_u64 v[16:17], v[10:11], 2, s[0:1]
	global_load_dword v12, v[16:17], off
	v_add_u32_e32 v8, 0x400, v2
	v_add_u32_e32 v10, 0x400, v3
	v_lshl_add_u64 v[16:17], v[8:9], 2, s[18:19]
	global_load_dword v237, v[16:17], off
	v_lshl_add_u64 v[16:17], v[10:11], 2, s[18:19]
	global_load_dword v241, v[16:17], off
	v_ashrrev_i32_e32 v8, 3, v8
	v_ashrrev_i32_e32 v10, 3, v10
	v_lshl_add_u64 v[16:17], v[8:9], 2, s[0:1]
	global_load_dword v245, v[16:17], off
	v_lshl_add_u64 v[16:17], v[10:11], 2, s[0:1]
	global_load_dword v13, v[16:17], off
	v_add_u32_e32 v8, 0x800, v2
	v_add_u32_e32 v10, 0x800, v3
	v_lshl_add_u64 v[16:17], v[8:9], 2, s[18:19]
	global_load_dword v238, v[16:17], off
	v_lshl_add_u64 v[16:17], v[10:11], 2, s[18:19]
	global_load_dword v242, v[16:17], off
	v_ashrrev_i32_e32 v8, 3, v8
	v_ashrrev_i32_e32 v10, 3, v10
	v_lshl_add_u64 v[16:17], v[8:9], 2, s[0:1]
	global_load_dword v246, v[16:17], off
	v_lshl_add_u64 v[16:17], v[10:11], 2, s[0:1]
	global_load_dword v14, v[16:17], off
	v_add_u32_e32 v8, 0xc00, v2
	v_add_u32_e32 v10, 0xc00, v3
	v_lshl_add_u64 v[16:17], v[8:9], 2, s[18:19]
	global_load_dword v239, v[16:17], off
	v_lshl_add_u64 v[16:17], v[10:11], 2, s[18:19]
	global_load_dword v243, v[16:17], off
	v_ashrrev_i32_e32 v8, 3, v8
	v_ashrrev_i32_e32 v10, 3, v10
	v_lshl_add_u64 v[16:17], v[8:9], 2, s[0:1]
	global_load_dword v247, v[16:17], off
	v_lshl_add_u64 v[16:17], v[10:11], 2, s[0:1]
	global_load_dword v15, v[16:17], off
	v_lshlrev_b32_e32 v1, 11, v2
	v_lshlrev_b32_e32 v7, 11, v3
	v_and_b32_e32 v1, 0x3800, v1
	v_and_b32_e32 v7, 0x3800, v7
	v_lshlrev_b32_e32 v1, 2, v1
	v_lshlrev_b32_e32 v7, 2, v7
	v_add_u32_e32 v6, -4, v6
	v_cmp_eq_u32_e32 vcc, 0, v6
	s_or_b64 s[22:23], vcc, s[22:23]
	s_waitcnt vmcnt(0)
	v_ashrrev_i32_e32 v8, 3, v2
	v_ashrrev_i32_e32 v10, 3, v3
	v_lshl_add_u32 v8, v8, 2, v1
	v_lshl_add_u32 v10, v10, 2, v7
	v_mul_f32_e32 v16, v236, v244
	v_mul_f32_e32 v17, v240, v12
	ds_write_b32 v8, v16
	ds_write_b32 v10, v17
	v_add_u32_e32 v8, 0x400, v2
	v_add_u32_e32 v10, 0x400, v3
	v_ashrrev_i32_e32 v8, 3, v8
	v_ashrrev_i32_e32 v10, 3, v10
	v_lshl_add_u32 v8, v8, 2, v1
	v_lshl_add_u32 v10, v10, 2, v7
	v_mul_f32_e32 v16, v237, v245
	v_mul_f32_e32 v17, v241, v13
	ds_write_b32 v8, v16
	ds_write_b32 v10, v17
	v_add_u32_e32 v8, 0x800, v2
	v_add_u32_e32 v10, 0x800, v3
	v_ashrrev_i32_e32 v8, 3, v8
	v_ashrrev_i32_e32 v10, 3, v10
	v_lshl_add_u32 v8, v8, 2, v1
	v_lshl_add_u32 v10, v10, 2, v7
	v_mul_f32_e32 v16, v238, v246
	v_mul_f32_e32 v17, v242, v14
	ds_write_b32 v8, v16
	ds_write_b32 v10, v17
	v_add_u32_e32 v8, 0xc00, v2
	v_add_u32_e32 v10, 0xc00, v3
	v_ashrrev_i32_e32 v8, 3, v8
	v_ashrrev_i32_e32 v10, 3, v10
	v_lshl_add_u32 v8, v8, 2, v1
	v_lshl_add_u32 v10, v10, 2, v7
	v_mul_f32_e32 v16, v239, v247
	v_mul_f32_e32 v17, v243, v15
	ds_write_b32 v8, v16
	ds_write_b32 v10, v17
	v_add_u32_e32 v3, 0x1000, v3
	v_add_u32_e32 v2, 0x1000, v2
	s_andn2_b64 exec, exec, s[22:23]
	s_cbranch_execnz .LBB0_1297
	s_or_b64 exec, exec, s[22:23]
